# expert-weight conversion: the per-tile LDS column-read section regenerated with 12 reads in flight (was 2, ~16 serialized LDS round trips per tile); same arithmetic; 115 converter workgroups
# baseline (speedup 1.0000x reference)
.Lmoe_w1:
	ds_write_b128 v142, v[2:5]
	s_waitcnt lgkmcnt(1)
	ds_write_b128 v142, v[6:9] offset:8192
	ds_write_b128 v142, v[10:13] offset:16384
	ds_write_b128 v142, v[14:17] offset:24576
	ds_write_b128 v142, v[18:21] offset:32768
	ds_write_b128 v142, v[22:25] offset:40960
	ds_write_b128 v142, v[26:29] offset:49152
	ds_write_b128 v142, v[30:33] offset:57344
	ds_write_b128 v143, v[34:37]
	ds_write_b128 v144, v[38:41]
	ds_write_b128 v145, v[42:45]
	ds_write_b128 v146, v[46:49]
	ds_write_b128 v147, v[50:53]
	ds_write_b128 v148, v[54:57]
	ds_write_b128 v149, v[58:61]
	ds_write_b128 v150, v[62:65]
	s_waitcnt lgkmcnt(0)
	s_barrier
	s_mov_b32 s100, 0x43000000
	s_mov_b32 s101, 0x43000000
	ds_read2st64_b32 v[202:203], v151 offset0:0 offset1:4
	ds_read2st64_b32 v[204:205], v151 offset0:8 offset1:12
	ds_read2st64_b32 v[206:207], v151 offset0:16 offset1:20
	ds_read2st64_b32 v[208:209], v151 offset0:24 offset1:28
	ds_read2st64_b32 v[210:211], v151 offset0:32 offset1:36
	ds_read2st64_b32 v[212:213], v151 offset0:40 offset1:44
	ds_read2st64_b32 v[214:215], v151 offset0:48 offset1:52
	ds_read2st64_b32 v[216:217], v151 offset0:56 offset1:60
	ds_read2st64_b32 v[218:219], v151 offset0:64 offset1:68
	ds_read2st64_b32 v[220:221], v151 offset0:72 offset1:76
	ds_read2st64_b32 v[222:223], v151 offset0:80 offset1:84
	ds_read2st64_b32 v[224:225], v151 offset0:88 offset1:92
	s_cmp_gt_i32 s10, 1
	s_waitcnt lgkmcnt(10)
	v_pk_mul_f32 v[202:203], v[202:203], s[100:101]
	v_pk_mul_f32 v[204:205], v[204:205], s[100:101]
	v_med3_f32 v202, v202, s11, v155
	v_med3_f32 v203, v203, s11, v155
	v_mov_b32_e32 v130, v135
	v_cvt_pk_fp8_f32 v130, v202, v203
	v_med3_f32 v204, v204, s11, v155
	v_med3_f32 v205, v205, s11, v155
	v_cvt_pk_fp8_f32 v130, v204, v205 op_sel:[0,0,1]
	ds_read2st64_b32 v[226:227], v151 offset0:96 offset1:100
	ds_read2st64_b32 v[228:229], v151 offset0:104 offset1:108
	s_waitcnt lgkmcnt(10)
	v_pk_mul_f32 v[206:207], v[206:207], s[100:101]
	v_pk_mul_f32 v[208:209], v[208:209], s[100:101]
	v_med3_f32 v206, v206, s11, v155
	v_med3_f32 v207, v207, s11, v155
	v_mov_b32_e32 v131, v135
	v_cvt_pk_fp8_f32 v131, v206, v207
	v_med3_f32 v208, v208, s11, v155
	v_med3_f32 v209, v209, s11, v155
	v_cvt_pk_fp8_f32 v131, v208, v209 op_sel:[0,0,1]
	ds_read2st64_b32 v[230:231], v151 offset0:112 offset1:116
	ds_read2st64_b32 v[232:233], v151 offset0:120 offset1:124
	s_waitcnt lgkmcnt(10)
	v_pk_mul_f32 v[210:211], v[210:211], s[100:101]
	v_pk_mul_f32 v[212:213], v[212:213], s[100:101]
	v_med3_f32 v210, v210, s11, v155
	v_med3_f32 v211, v211, s11, v155
	v_mov_b32_e32 v132, v135
	v_cvt_pk_fp8_f32 v132, v210, v211
	v_med3_f32 v212, v212, s11, v155
	v_med3_f32 v213, v213, s11, v155
	v_cvt_pk_fp8_f32 v132, v212, v213 op_sel:[0,0,1]
	ds_read2st64_b32 v[202:203], v151 offset0:128 offset1:132
	ds_read2st64_b32 v[204:205], v151 offset0:136 offset1:140
	s_waitcnt lgkmcnt(10)
	v_pk_mul_f32 v[214:215], v[214:215], s[100:101]
	v_pk_mul_f32 v[216:217], v[216:217], s[100:101]
	v_med3_f32 v214, v214, s11, v155
	v_med3_f32 v215, v215, s11, v155
	v_mov_b32_e32 v133, v135
	v_cvt_pk_fp8_f32 v133, v214, v215
	v_med3_f32 v216, v216, s11, v155
	v_med3_f32 v217, v217, s11, v155
	v_cvt_pk_fp8_f32 v133, v216, v217 op_sel:[0,0,1]
	ds_read2st64_b32 v[206:207], v151 offset0:144 offset1:148
	ds_read2st64_b32 v[208:209], v151 offset0:152 offset1:156
	s_waitcnt lgkmcnt(10)
	v_pk_mul_f32 v[218:219], v[218:219], s[100:101]
	v_pk_mul_f32 v[220:221], v[220:221], s[100:101]
	v_med3_f32 v218, v218, s11, v155
	v_med3_f32 v219, v219, s11, v155
	v_mov_b32_e32 v164, v135
	v_cvt_pk_fp8_f32 v164, v218, v219
	v_med3_f32 v220, v220, s11, v155
	v_med3_f32 v221, v221, s11, v155
	v_cvt_pk_fp8_f32 v164, v220, v221 op_sel:[0,0,1]
	ds_read2st64_b32 v[210:211], v151 offset0:160 offset1:164
	ds_read2st64_b32 v[212:213], v151 offset0:168 offset1:172
	s_waitcnt lgkmcnt(10)
	v_pk_mul_f32 v[222:223], v[222:223], s[100:101]
	v_pk_mul_f32 v[224:225], v[224:225], s[100:101]
	v_med3_f32 v222, v222, s11, v155
	v_med3_f32 v223, v223, s11, v155
	v_mov_b32_e32 v165, v135
	v_cvt_pk_fp8_f32 v165, v222, v223
	v_med3_f32 v224, v224, s11, v155
	v_med3_f32 v225, v225, s11, v155
	v_cvt_pk_fp8_f32 v165, v224, v225 op_sel:[0,0,1]
	ds_read2st64_b32 v[214:215], v151 offset0:176 offset1:180
	ds_read2st64_b32 v[216:217], v151 offset0:184 offset1:188
	s_waitcnt lgkmcnt(10)
	v_pk_mul_f32 v[226:227], v[226:227], s[100:101]
	v_pk_mul_f32 v[228:229], v[228:229], s[100:101]
	v_med3_f32 v226, v226, s11, v155
	v_med3_f32 v227, v227, s11, v155
	v_mov_b32_e32 v166, v135
	v_cvt_pk_fp8_f32 v166, v226, v227
	v_med3_f32 v228, v228, s11, v155
	v_med3_f32 v229, v229, s11, v155
	v_cvt_pk_fp8_f32 v166, v228, v229 op_sel:[0,0,1]
	ds_read2st64_b32 v[218:219], v151 offset0:192 offset1:196
	ds_read2st64_b32 v[220:221], v151 offset0:200 offset1:204
	s_waitcnt lgkmcnt(10)
	v_pk_mul_f32 v[230:231], v[230:231], s[100:101]
	v_pk_mul_f32 v[232:233], v[232:233], s[100:101]
	v_med3_f32 v230, v230, s11, v155
	v_med3_f32 v231, v231, s11, v155
	v_mov_b32_e32 v167, v135
	v_cvt_pk_fp8_f32 v167, v230, v231
	v_med3_f32 v232, v232, s11, v155
	v_med3_f32 v233, v233, s11, v155
	v_cvt_pk_fp8_f32 v167, v232, v233 op_sel:[0,0,1]
	ds_read2st64_b32 v[222:223], v151 offset0:208 offset1:212
	ds_read2st64_b32 v[224:225], v151 offset0:216 offset1:220
	s_waitcnt lgkmcnt(10)
	v_pk_mul_f32 v[202:203], v[202:203], s[100:101]
	v_pk_mul_f32 v[204:205], v[204:205], s[100:101]
	v_med3_f32 v202, v202, s11, v155
	v_med3_f32 v203, v203, s11, v155
	v_mov_b32_e32 v168, v135
	v_cvt_pk_fp8_f32 v168, v202, v203
	v_med3_f32 v204, v204, s11, v155
	v_med3_f32 v205, v205, s11, v155
	v_cvt_pk_fp8_f32 v168, v204, v205 op_sel:[0,0,1]
	ds_read2st64_b32 v[226:227], v151 offset0:224 offset1:228
	ds_read2st64_b32 v[228:229], v151 offset0:232 offset1:236
	s_waitcnt lgkmcnt(10)
	v_pk_mul_f32 v[206:207], v[206:207], s[100:101]
	v_pk_mul_f32 v[208:209], v[208:209], s[100:101]
	v_med3_f32 v206, v206, s11, v155
	v_med3_f32 v207, v207, s11, v155
	v_mov_b32_e32 v169, v135
	v_cvt_pk_fp8_f32 v169, v206, v207
	v_med3_f32 v208, v208, s11, v155
	v_med3_f32 v209, v209, s11, v155
	v_cvt_pk_fp8_f32 v169, v208, v209 op_sel:[0,0,1]
	ds_read2st64_b32 v[230:231], v151 offset0:240 offset1:244
	ds_read2st64_b32 v[232:233], v151 offset0:248 offset1:252
	s_waitcnt lgkmcnt(10)
	v_pk_mul_f32 v[210:211], v[210:211], s[100:101]
	v_pk_mul_f32 v[212:213], v[212:213], s[100:101]
	v_med3_f32 v210, v210, s11, v155
	v_med3_f32 v211, v211, s11, v155
	v_mov_b32_e32 v170, v135
	v_cvt_pk_fp8_f32 v170, v210, v211
	v_med3_f32 v212, v212, s11, v155
	v_med3_f32 v213, v213, s11, v155
	v_cvt_pk_fp8_f32 v170, v212, v213 op_sel:[0,0,1]
	s_waitcnt lgkmcnt(8)
	v_pk_mul_f32 v[214:215], v[214:215], s[100:101]
	v_pk_mul_f32 v[216:217], v[216:217], s[100:101]
	v_med3_f32 v214, v214, s11, v155
	v_med3_f32 v215, v215, s11, v155
	v_mov_b32_e32 v171, v135
	v_cvt_pk_fp8_f32 v171, v214, v215
	v_med3_f32 v216, v216, s11, v155
	v_med3_f32 v217, v217, s11, v155
	v_cvt_pk_fp8_f32 v171, v216, v217 op_sel:[0,0,1]
	s_waitcnt lgkmcnt(6)
	v_pk_mul_f32 v[218:219], v[218:219], s[100:101]
	v_pk_mul_f32 v[220:221], v[220:221], s[100:101]
	v_med3_f32 v218, v218, s11, v155
	v_med3_f32 v219, v219, s11, v155
	v_mov_b32_e32 v172, v135
	v_cvt_pk_fp8_f32 v172, v218, v219
	v_med3_f32 v220, v220, s11, v155
	v_med3_f32 v221, v221, s11, v155
	v_cvt_pk_fp8_f32 v172, v220, v221 op_sel:[0,0,1]
	s_waitcnt lgkmcnt(4)
	v_pk_mul_f32 v[222:223], v[222:223], s[100:101]
	v_pk_mul_f32 v[224:225], v[224:225], s[100:101]
	v_med3_f32 v222, v222, s11, v155
	v_med3_f32 v223, v223, s11, v155
	v_mov_b32_e32 v173, v135
	v_cvt_pk_fp8_f32 v173, v222, v223
	v_med3_f32 v224, v224, s11, v155
	v_med3_f32 v225, v225, s11, v155
	v_cvt_pk_fp8_f32 v173, v224, v225 op_sel:[0,0,1]
	s_waitcnt lgkmcnt(2)
	v_pk_mul_f32 v[226:227], v[226:227], s[100:101]
	v_pk_mul_f32 v[228:229], v[228:229], s[100:101]
	v_med3_f32 v226, v226, s11, v155
	v_med3_f32 v227, v227, s11, v155
	v_mov_b32_e32 v174, v135
	v_cvt_pk_fp8_f32 v174, v226, v227
	v_med3_f32 v228, v228, s11, v155
	v_med3_f32 v229, v229, s11, v155
	v_cvt_pk_fp8_f32 v174, v228, v229 op_sel:[0,0,1]
	s_waitcnt lgkmcnt(0)
	v_pk_mul_f32 v[230:231], v[230:231], s[100:101]
	v_pk_mul_f32 v[232:233], v[232:233], s[100:101]
	v_med3_f32 v230, v230, s11, v155
	v_med3_f32 v231, v231, s11, v155
	v_mov_b32_e32 v175, v135
	v_cvt_pk_fp8_f32 v175, v230, v231
	v_med3_f32 v232, v232, s11, v155
	v_med3_f32 v233, v233, s11, v155
	v_cvt_pk_fp8_f32 v175, v232, v233 op_sel:[0,0,1]
	s_barrier
	ds_write_b128 v156, v[130:133]
	ds_write_b128 v157, v[164:167]
	ds_write_b128 v158, v[168:171]
	ds_write_b128 v159, v[172:175]
	s_waitcnt lgkmcnt(0)
	s_barrier
	ds_read_b128 v[130:133], v160
	v_add_u32_e32 v164, s4, v140
	s_cselect_b64 s[46:47], -1, 0
	s_mov_b64 s[2:3], -1
	s_and_b64 vcc, exec, s[46:47]
	v_lshlrev_b32_e32 v165, 1, v164
	v_add_u32_e32 v137, s0, v138
	s_cbranch_vccz .LBB0_380
	v_lshlrev_b32_e32 v134, 2, v164
	v_lshrrev_b32_e32 v166, 1, v164
	v_and_b32_e32 v167, 0xffffffe3, v164
	v_and_or_b32 v168, v166, 12, v167
	v_and_or_b32 v169, v134, 16, v167
	v_ashrrev_i32_e32 v166, 7, v164
	v_ashrrev_i32_e32 v134, 7, v137
	v_mad_u64_u32 v[166:167], s[2:3], v166, 56, v[134:135]
	v_lshrrev_b32_e32 v134, 3, v169
	v_bfe_u32 v169, v137, 6, 1
	v_ashrrev_i32_e32 v167, 31, v166
	v_and_or_b32 v134, v134, 14, v169
	v_lshlrev_b32_e32 v168, 6, v168
	v_and_b32_e32 v169, 63, v137
	v_lshlrev_b64 v[166:167], 14, v[166:167]
	v_and_or_b32 v168, v168, s16, v169
	v_lshlrev_b32_e32 v134, 10, v134
	v_and_b32_e32 v169, 32, v165
	v_bitop3_b32 v134, v134, v168, v169 bitop3:0xf6
	v_lshl_add_u64 v[166:167], s[6:7], 0, v[166:167]
	v_lshl_add_u64 v[166:167], v[166:167], 0, v[134:135]
	s_waitcnt lgkmcnt(0)
	global_store_dwordx4 v[166:167], v[130:133], off nt
	s_mov_b64 s[2:3], 0

.Lmoe_w2:
	ds_write_b128 v142, v[66:69]
	ds_write_b128 v142, v[70:73] offset:8192
	ds_write_b128 v142, v[74:77] offset:16384
	ds_write_b128 v142, v[78:81] offset:24576
	ds_write_b128 v142, v[82:85] offset:32768
	ds_write_b128 v142, v[86:89] offset:40960
	ds_write_b128 v142, v[90:93] offset:49152
	ds_write_b128 v142, v[94:97] offset:57344
	ds_write_b128 v143, v[98:101]
	ds_write_b128 v144, v[102:105]
	ds_write_b128 v145, v[106:109]
	ds_write_b128 v146, v[110:113]
	ds_write_b128 v147, v[114:117]
	ds_write_b128 v148, v[118:121]
	ds_write_b128 v149, v[122:125]
	ds_write_b128 v150, v[126:129]
	s_waitcnt lgkmcnt(0)
	s_barrier
	s_mov_b32 s100, 0x43000000
	s_mov_b32 s101, 0x43000000
	ds_read2st64_b32 v[202:203], v151 offset0:0 offset1:4
	ds_read2st64_b32 v[204:205], v151 offset0:8 offset1:12
	ds_read2st64_b32 v[206:207], v151 offset0:16 offset1:20
	ds_read2st64_b32 v[208:209], v151 offset0:24 offset1:28
	ds_read2st64_b32 v[210:211], v151 offset0:32 offset1:36
	ds_read2st64_b32 v[212:213], v151 offset0:40 offset1:44
	ds_read2st64_b32 v[214:215], v151 offset0:48 offset1:52
	ds_read2st64_b32 v[216:217], v151 offset0:56 offset1:60
	ds_read2st64_b32 v[218:219], v151 offset0:64 offset1:68
	ds_read2st64_b32 v[220:221], v151 offset0:72 offset1:76
	ds_read2st64_b32 v[222:223], v151 offset0:80 offset1:84
	ds_read2st64_b32 v[224:225], v151 offset0:88 offset1:92
	s_cmp_gt_i32 s17, 1
	s_waitcnt lgkmcnt(10)
	v_pk_mul_f32 v[202:203], v[202:203], s[100:101]
	v_pk_mul_f32 v[204:205], v[204:205], s[100:101]
	v_med3_f32 v202, v202, s11, v155
	v_med3_f32 v203, v203, s11, v155
	v_mov_b32_e32 v130, v135
	v_cvt_pk_fp8_f32 v130, v202, v203
	v_med3_f32 v204, v204, s11, v155
	v_med3_f32 v205, v205, s11, v155
	v_cvt_pk_fp8_f32 v130, v204, v205 op_sel:[0,0,1]
	ds_read2st64_b32 v[226:227], v151 offset0:96 offset1:100
	ds_read2st64_b32 v[228:229], v151 offset0:104 offset1:108
	s_waitcnt lgkmcnt(10)
	v_pk_mul_f32 v[206:207], v[206:207], s[100:101]
	v_pk_mul_f32 v[208:209], v[208:209], s[100:101]
	v_med3_f32 v206, v206, s11, v155
	v_med3_f32 v207, v207, s11, v155
	v_mov_b32_e32 v131, v135
	v_cvt_pk_fp8_f32 v131, v206, v207
	v_med3_f32 v208, v208, s11, v155
	v_med3_f32 v209, v209, s11, v155
	v_cvt_pk_fp8_f32 v131, v208, v209 op_sel:[0,0,1]
	ds_read2st64_b32 v[230:231], v151 offset0:112 offset1:116
	ds_read2st64_b32 v[232:233], v151 offset0:120 offset1:124
	s_waitcnt lgkmcnt(10)
	v_pk_mul_f32 v[210:211], v[210:211], s[100:101]
	v_pk_mul_f32 v[212:213], v[212:213], s[100:101]
	v_med3_f32 v210, v210, s11, v155
	v_med3_f32 v211, v211, s11, v155
	v_mov_b32_e32 v132, v135
	v_cvt_pk_fp8_f32 v132, v210, v211
	v_med3_f32 v212, v212, s11, v155
	v_med3_f32 v213, v213, s11, v155
	v_cvt_pk_fp8_f32 v132, v212, v213 op_sel:[0,0,1]
	ds_read2st64_b32 v[202:203], v151 offset0:128 offset1:132
	ds_read2st64_b32 v[204:205], v151 offset0:136 offset1:140
	s_waitcnt lgkmcnt(10)
	v_pk_mul_f32 v[214:215], v[214:215], s[100:101]
	v_pk_mul_f32 v[216:217], v[216:217], s[100:101]
	v_med3_f32 v214, v214, s11, v155
	v_med3_f32 v215, v215, s11, v155
	v_mov_b32_e32 v133, v135
	v_cvt_pk_fp8_f32 v133, v214, v215
	v_med3_f32 v216, v216, s11, v155
	v_med3_f32 v217, v217, s11, v155
	v_cvt_pk_fp8_f32 v133, v216, v217 op_sel:[0,0,1]
	ds_read2st64_b32 v[206:207], v151 offset0:144 offset1:148
	ds_read2st64_b32 v[208:209], v151 offset0:152 offset1:156
	s_waitcnt lgkmcnt(10)
	v_pk_mul_f32 v[218:219], v[218:219], s[100:101]
	v_pk_mul_f32 v[220:221], v[220:221], s[100:101]
	v_med3_f32 v218, v218, s11, v155
	v_med3_f32 v219, v219, s11, v155
	v_mov_b32_e32 v164, v135
	v_cvt_pk_fp8_f32 v164, v218, v219
	v_med3_f32 v220, v220, s11, v155
	v_med3_f32 v221, v221, s11, v155
	v_cvt_pk_fp8_f32 v164, v220, v221 op_sel:[0,0,1]
	ds_read2st64_b32 v[210:211], v151 offset0:160 offset1:164
	ds_read2st64_b32 v[212:213], v151 offset0:168 offset1:172
	s_waitcnt lgkmcnt(10)
	v_pk_mul_f32 v[222:223], v[222:223], s[100:101]
	v_pk_mul_f32 v[224:225], v[224:225], s[100:101]
	v_med3_f32 v222, v222, s11, v155
	v_med3_f32 v223, v223, s11, v155
	v_mov_b32_e32 v165, v135
	v_cvt_pk_fp8_f32 v165, v222, v223
	v_med3_f32 v224, v224, s11, v155
	v_med3_f32 v225, v225, s11, v155
	v_cvt_pk_fp8_f32 v165, v224, v225 op_sel:[0,0,1]
	ds_read2st64_b32 v[214:215], v151 offset0:176 offset1:180
	ds_read2st64_b32 v[216:217], v151 offset0:184 offset1:188
	s_waitcnt lgkmcnt(10)
	v_pk_mul_f32 v[226:227], v[226:227], s[100:101]
	v_pk_mul_f32 v[228:229], v[228:229], s[100:101]
	v_med3_f32 v226, v226, s11, v155
	v_med3_f32 v227, v227, s11, v155
	v_mov_b32_e32 v166, v135
	v_cvt_pk_fp8_f32 v166, v226, v227
	v_med3_f32 v228, v228, s11, v155
	v_med3_f32 v229, v229, s11, v155
	v_cvt_pk_fp8_f32 v166, v228, v229 op_sel:[0,0,1]
	ds_read2st64_b32 v[218:219], v151 offset0:192 offset1:196
	ds_read2st64_b32 v[220:221], v151 offset0:200 offset1:204
	s_waitcnt lgkmcnt(10)
	v_pk_mul_f32 v[230:231], v[230:231], s[100:101]
	v_pk_mul_f32 v[232:233], v[232:233], s[100:101]
	v_med3_f32 v230, v230, s11, v155
	v_med3_f32 v231, v231, s11, v155
	v_mov_b32_e32 v167, v135
	v_cvt_pk_fp8_f32 v167, v230, v231
	v_med3_f32 v232, v232, s11, v155
	v_med3_f32 v233, v233, s11, v155
	v_cvt_pk_fp8_f32 v167, v232, v233 op_sel:[0,0,1]
	ds_read2st64_b32 v[222:223], v151 offset0:208 offset1:212
	ds_read2st64_b32 v[224:225], v151 offset0:216 offset1:220
	s_waitcnt lgkmcnt(10)
	v_pk_mul_f32 v[202:203], v[202:203], s[100:101]
	v_pk_mul_f32 v[204:205], v[204:205], s[100:101]
	v_med3_f32 v202, v202, s11, v155
	v_med3_f32 v203, v203, s11, v155
	v_mov_b32_e32 v168, v135
	v_cvt_pk_fp8_f32 v168, v202, v203
	v_med3_f32 v204, v204, s11, v155
	v_med3_f32 v205, v205, s11, v155
	v_cvt_pk_fp8_f32 v168, v204, v205 op_sel:[0,0,1]
	ds_read2st64_b32 v[226:227], v151 offset0:224 offset1:228
	ds_read2st64_b32 v[228:229], v151 offset0:232 offset1:236
	s_waitcnt lgkmcnt(10)
	v_pk_mul_f32 v[206:207], v[206:207], s[100:101]
	v_pk_mul_f32 v[208:209], v[208:209], s[100:101]
	v_med3_f32 v206, v206, s11, v155
	v_med3_f32 v207, v207, s11, v155
	v_mov_b32_e32 v169, v135
	v_cvt_pk_fp8_f32 v169, v206, v207
	v_med3_f32 v208, v208, s11, v155
	v_med3_f32 v209, v209, s11, v155
	v_cvt_pk_fp8_f32 v169, v208, v209 op_sel:[0,0,1]
	ds_read2st64_b32 v[230:231], v151 offset0:240 offset1:244
	ds_read2st64_b32 v[232:233], v151 offset0:248 offset1:252
	s_waitcnt lgkmcnt(10)
	v_pk_mul_f32 v[210:211], v[210:211], s[100:101]
	v_pk_mul_f32 v[212:213], v[212:213], s[100:101]
	v_med3_f32 v210, v210, s11, v155
	v_med3_f32 v211, v211, s11, v155
	v_mov_b32_e32 v170, v135
	v_cvt_pk_fp8_f32 v170, v210, v211
	v_med3_f32 v212, v212, s11, v155
	v_med3_f32 v213, v213, s11, v155
	v_cvt_pk_fp8_f32 v170, v212, v213 op_sel:[0,0,1]
	s_waitcnt lgkmcnt(8)
	v_pk_mul_f32 v[214:215], v[214:215], s[100:101]
	v_pk_mul_f32 v[216:217], v[216:217], s[100:101]
	v_med3_f32 v214, v214, s11, v155
	v_med3_f32 v215, v215, s11, v155
	v_mov_b32_e32 v171, v135
	v_cvt_pk_fp8_f32 v171, v214, v215
	v_med3_f32 v216, v216, s11, v155
	v_med3_f32 v217, v217, s11, v155
	v_cvt_pk_fp8_f32 v171, v216, v217 op_sel:[0,0,1]
	s_waitcnt lgkmcnt(6)
	v_pk_mul_f32 v[218:219], v[218:219], s[100:101]
	v_pk_mul_f32 v[220:221], v[220:221], s[100:101]
	v_med3_f32 v218, v218, s11, v155
	v_med3_f32 v219, v219, s11, v155
	v_mov_b32_e32 v172, v135
	v_cvt_pk_fp8_f32 v172, v218, v219
	v_med3_f32 v220, v220, s11, v155
	v_med3_f32 v221, v221, s11, v155
	v_cvt_pk_fp8_f32 v172, v220, v221 op_sel:[0,0,1]
	s_waitcnt lgkmcnt(4)
	v_pk_mul_f32 v[222:223], v[222:223], s[100:101]
	v_pk_mul_f32 v[224:225], v[224:225], s[100:101]
	v_med3_f32 v222, v222, s11, v155
	v_med3_f32 v223, v223, s11, v155
	v_mov_b32_e32 v173, v135
	v_cvt_pk_fp8_f32 v173, v222, v223
	v_med3_f32 v224, v224, s11, v155
	v_med3_f32 v225, v225, s11, v155
	v_cvt_pk_fp8_f32 v173, v224, v225 op_sel:[0,0,1]
	s_waitcnt lgkmcnt(2)
	v_pk_mul_f32 v[226:227], v[226:227], s[100:101]
	v_pk_mul_f32 v[228:229], v[228:229], s[100:101]
	v_med3_f32 v226, v226, s11, v155
	v_med3_f32 v227, v227, s11, v155
	v_mov_b32_e32 v174, v135
	v_cvt_pk_fp8_f32 v174, v226, v227
	v_med3_f32 v228, v228, s11, v155
	v_med3_f32 v229, v229, s11, v155
	v_cvt_pk_fp8_f32 v174, v228, v229 op_sel:[0,0,1]
	s_waitcnt lgkmcnt(0)
	v_pk_mul_f32 v[230:231], v[230:231], s[100:101]
	v_pk_mul_f32 v[232:233], v[232:233], s[100:101]
	v_med3_f32 v230, v230, s11, v155
	v_med3_f32 v231, v231, s11, v155
	v_mov_b32_e32 v175, v135
	v_cvt_pk_fp8_f32 v175, v230, v231
	v_med3_f32 v232, v232, s11, v155
	v_med3_f32 v233, v233, s11, v155
	v_cvt_pk_fp8_f32 v175, v232, v233 op_sel:[0,0,1]
	s_barrier
	ds_write_b128 v156, v[130:133]
	ds_write_b128 v157, v[164:167]
	ds_write_b128 v158, v[168:171]
	ds_write_b128 v159, v[172:175]
	s_waitcnt lgkmcnt(0)
	s_barrier
	ds_read_b128 v[130:133], v160
	v_add_u32_e32 v164, s36, v140
	s_cselect_b64 s[44:45], -1, 0
	s_mov_b64 s[2:3], -1
	s_and_b64 vcc, exec, s[44:45]
	v_lshlrev_b32_e32 v165, 1, v164
	v_add_u32_e32 v137, s14, v138
	s_cbranch_vccz .LBB0_404
	v_lshlrev_b32_e32 v134, 2, v164
	v_lshrrev_b32_e32 v166, 1, v164
	v_and_b32_e32 v167, 0xffffffe3, v164
	v_and_or_b32 v168, v166, 12, v167
	v_and_or_b32 v169, v134, 16, v167
	v_ashrrev_i32_e32 v166, 7, v164
	v_ashrrev_i32_e32 v134, 7, v137
	v_mad_u64_u32 v[166:167], s[2:3], v166, 56, v[134:135]
	v_lshrrev_b32_e32 v134, 3, v169
	v_bfe_u32 v169, v137, 6, 1
	v_ashrrev_i32_e32 v167, 31, v166
	v_and_or_b32 v134, v134, 14, v169
	v_lshlrev_b32_e32 v168, 6, v168
	v_and_b32_e32 v169, 63, v137
	v_lshlrev_b64 v[166:167], 14, v[166:167]
	v_and_or_b32 v168, v168, s16, v169
	v_lshlrev_b32_e32 v134, 10, v134
	v_and_b32_e32 v169, 32, v165
	v_bitop3_b32 v134, v134, v168, v169 bitop3:0xf6
	v_lshl_add_u64 v[166:167], s[40:41], 0, v[166:167]
	v_lshl_add_u64 v[166:167], v[166:167], 0, v[134:135]
	s_waitcnt lgkmcnt(0)
	global_store_dwordx4 v[166:167], v[130:133], off nt
	s_mov_b64 s[2:3], 0

.Lcv_moe_w1:
	ds_write_b128 v142, v[2:5]
	s_waitcnt lgkmcnt(1)
	ds_write_b128 v142, v[6:9] offset:8192
	ds_write_b128 v142, v[10:13] offset:16384
	ds_write_b128 v142, v[14:17] offset:24576
	ds_write_b128 v142, v[18:21] offset:32768
	ds_write_b128 v142, v[22:25] offset:40960
	ds_write_b128 v142, v[26:29] offset:49152
	ds_write_b128 v142, v[30:33] offset:57344
	ds_write_b128 v143, v[34:37]
	ds_write_b128 v144, v[38:41]
	ds_write_b128 v145, v[42:45]
	ds_write_b128 v146, v[46:49]
	ds_write_b128 v147, v[50:53]
	ds_write_b128 v148, v[54:57]
	ds_write_b128 v149, v[58:61]
	ds_write_b128 v150, v[62:65]
	s_waitcnt lgkmcnt(0)
	s_barrier
	s_mov_b32 s100, 0x43000000
	s_mov_b32 s101, 0x43000000
	ds_read2st64_b32 v[202:203], v151 offset0:0 offset1:4
	ds_read2st64_b32 v[204:205], v151 offset0:8 offset1:12
	ds_read2st64_b32 v[206:207], v151 offset0:16 offset1:20
	ds_read2st64_b32 v[208:209], v151 offset0:24 offset1:28
	ds_read2st64_b32 v[210:211], v151 offset0:32 offset1:36
	ds_read2st64_b32 v[212:213], v151 offset0:40 offset1:44
	ds_read2st64_b32 v[214:215], v151 offset0:48 offset1:52
	ds_read2st64_b32 v[216:217], v151 offset0:56 offset1:60
	ds_read2st64_b32 v[218:219], v151 offset0:64 offset1:68
	ds_read2st64_b32 v[220:221], v151 offset0:72 offset1:76
	ds_read2st64_b32 v[222:223], v151 offset0:80 offset1:84
	ds_read2st64_b32 v[224:225], v151 offset0:88 offset1:92
	s_cmp_gt_i32 s10, 1
	s_waitcnt lgkmcnt(10)
	v_pk_mul_f32 v[202:203], v[202:203], s[100:101]
	v_pk_mul_f32 v[204:205], v[204:205], s[100:101]
	v_med3_f32 v202, v202, s11, v155
	v_med3_f32 v203, v203, s11, v155
	v_mov_b32_e32 v130, v135
	v_cvt_pk_fp8_f32 v130, v202, v203
	v_med3_f32 v204, v204, s11, v155
	v_med3_f32 v205, v205, s11, v155
	v_cvt_pk_fp8_f32 v130, v204, v205 op_sel:[0,0,1]
	ds_read2st64_b32 v[226:227], v151 offset0:96 offset1:100
	ds_read2st64_b32 v[228:229], v151 offset0:104 offset1:108
	s_waitcnt lgkmcnt(10)
	v_pk_mul_f32 v[206:207], v[206:207], s[100:101]
	v_pk_mul_f32 v[208:209], v[208:209], s[100:101]
	v_med3_f32 v206, v206, s11, v155
	v_med3_f32 v207, v207, s11, v155
	v_mov_b32_e32 v131, v135
	v_cvt_pk_fp8_f32 v131, v206, v207
	v_med3_f32 v208, v208, s11, v155
	v_med3_f32 v209, v209, s11, v155
	v_cvt_pk_fp8_f32 v131, v208, v209 op_sel:[0,0,1]
	ds_read2st64_b32 v[230:231], v151 offset0:112 offset1:116
	ds_read2st64_b32 v[232:233], v151 offset0:120 offset1:124
	s_waitcnt lgkmcnt(10)
	v_pk_mul_f32 v[210:211], v[210:211], s[100:101]
	v_pk_mul_f32 v[212:213], v[212:213], s[100:101]
	v_med3_f32 v210, v210, s11, v155
	v_med3_f32 v211, v211, s11, v155
	v_mov_b32_e32 v132, v135
	v_cvt_pk_fp8_f32 v132, v210, v211
	v_med3_f32 v212, v212, s11, v155
	v_med3_f32 v213, v213, s11, v155
	v_cvt_pk_fp8_f32 v132, v212, v213 op_sel:[0,0,1]
	ds_read2st64_b32 v[202:203], v151 offset0:128 offset1:132
	ds_read2st64_b32 v[204:205], v151 offset0:136 offset1:140
	s_waitcnt lgkmcnt(10)
	v_pk_mul_f32 v[214:215], v[214:215], s[100:101]
	v_pk_mul_f32 v[216:217], v[216:217], s[100:101]
	v_med3_f32 v214, v214, s11, v155
	v_med3_f32 v215, v215, s11, v155
	v_mov_b32_e32 v133, v135
	v_cvt_pk_fp8_f32 v133, v214, v215
	v_med3_f32 v216, v216, s11, v155
	v_med3_f32 v217, v217, s11, v155
	v_cvt_pk_fp8_f32 v133, v216, v217 op_sel:[0,0,1]
	ds_read2st64_b32 v[206:207], v151 offset0:144 offset1:148
	ds_read2st64_b32 v[208:209], v151 offset0:152 offset1:156
	s_waitcnt lgkmcnt(10)
	v_pk_mul_f32 v[218:219], v[218:219], s[100:101]
	v_pk_mul_f32 v[220:221], v[220:221], s[100:101]
	v_med3_f32 v218, v218, s11, v155
	v_med3_f32 v219, v219, s11, v155
	v_mov_b32_e32 v164, v135
	v_cvt_pk_fp8_f32 v164, v218, v219
	v_med3_f32 v220, v220, s11, v155
	v_med3_f32 v221, v221, s11, v155
	v_cvt_pk_fp8_f32 v164, v220, v221 op_sel:[0,0,1]
	ds_read2st64_b32 v[210:211], v151 offset0:160 offset1:164
	ds_read2st64_b32 v[212:213], v151 offset0:168 offset1:172
	s_waitcnt lgkmcnt(10)
	v_pk_mul_f32 v[222:223], v[222:223], s[100:101]
	v_pk_mul_f32 v[224:225], v[224:225], s[100:101]
	v_med3_f32 v222, v222, s11, v155
	v_med3_f32 v223, v223, s11, v155
	v_mov_b32_e32 v165, v135
	v_cvt_pk_fp8_f32 v165, v222, v223
	v_med3_f32 v224, v224, s11, v155
	v_med3_f32 v225, v225, s11, v155
	v_cvt_pk_fp8_f32 v165, v224, v225 op_sel:[0,0,1]
	ds_read2st64_b32 v[214:215], v151 offset0:176 offset1:180
	ds_read2st64_b32 v[216:217], v151 offset0:184 offset1:188
	s_waitcnt lgkmcnt(10)
	v_pk_mul_f32 v[226:227], v[226:227], s[100:101]
	v_pk_mul_f32 v[228:229], v[228:229], s[100:101]
	v_med3_f32 v226, v226, s11, v155
	v_med3_f32 v227, v227, s11, v155
	v_mov_b32_e32 v166, v135
	v_cvt_pk_fp8_f32 v166, v226, v227
	v_med3_f32 v228, v228, s11, v155
	v_med3_f32 v229, v229, s11, v155
	v_cvt_pk_fp8_f32 v166, v228, v229 op_sel:[0,0,1]
	ds_read2st64_b32 v[218:219], v151 offset0:192 offset1:196
	ds_read2st64_b32 v[220:221], v151 offset0:200 offset1:204
	s_waitcnt lgkmcnt(10)
	v_pk_mul_f32 v[230:231], v[230:231], s[100:101]
	v_pk_mul_f32 v[232:233], v[232:233], s[100:101]
	v_med3_f32 v230, v230, s11, v155
	v_med3_f32 v231, v231, s11, v155
	v_mov_b32_e32 v167, v135
	v_cvt_pk_fp8_f32 v167, v230, v231
	v_med3_f32 v232, v232, s11, v155
	v_med3_f32 v233, v233, s11, v155
	v_cvt_pk_fp8_f32 v167, v232, v233 op_sel:[0,0,1]
	ds_read2st64_b32 v[222:223], v151 offset0:208 offset1:212
	ds_read2st64_b32 v[224:225], v151 offset0:216 offset1:220
	s_waitcnt lgkmcnt(10)
	v_pk_mul_f32 v[202:203], v[202:203], s[100:101]
	v_pk_mul_f32 v[204:205], v[204:205], s[100:101]
	v_med3_f32 v202, v202, s11, v155
	v_med3_f32 v203, v203, s11, v155
	v_mov_b32_e32 v168, v135
	v_cvt_pk_fp8_f32 v168, v202, v203
	v_med3_f32 v204, v204, s11, v155
	v_med3_f32 v205, v205, s11, v155
	v_cvt_pk_fp8_f32 v168, v204, v205 op_sel:[0,0,1]
	ds_read2st64_b32 v[226:227], v151 offset0:224 offset1:228
	ds_read2st64_b32 v[228:229], v151 offset0:232 offset1:236
	s_waitcnt lgkmcnt(10)
	v_pk_mul_f32 v[206:207], v[206:207], s[100:101]
	v_pk_mul_f32 v[208:209], v[208:209], s[100:101]
	v_med3_f32 v206, v206, s11, v155
	v_med3_f32 v207, v207, s11, v155
	v_mov_b32_e32 v169, v135
	v_cvt_pk_fp8_f32 v169, v206, v207
	v_med3_f32 v208, v208, s11, v155
	v_med3_f32 v209, v209, s11, v155
	v_cvt_pk_fp8_f32 v169, v208, v209 op_sel:[0,0,1]
	ds_read2st64_b32 v[230:231], v151 offset0:240 offset1:244
	ds_read2st64_b32 v[232:233], v151 offset0:248 offset1:252
	s_waitcnt lgkmcnt(10)
	v_pk_mul_f32 v[210:211], v[210:211], s[100:101]
	v_pk_mul_f32 v[212:213], v[212:213], s[100:101]
	v_med3_f32 v210, v210, s11, v155
	v_med3_f32 v211, v211, s11, v155
	v_mov_b32_e32 v170, v135
	v_cvt_pk_fp8_f32 v170, v210, v211
	v_med3_f32 v212, v212, s11, v155
	v_med3_f32 v213, v213, s11, v155
	v_cvt_pk_fp8_f32 v170, v212, v213 op_sel:[0,0,1]
	s_waitcnt lgkmcnt(8)
	v_pk_mul_f32 v[214:215], v[214:215], s[100:101]
	v_pk_mul_f32 v[216:217], v[216:217], s[100:101]
	v_med3_f32 v214, v214, s11, v155
	v_med3_f32 v215, v215, s11, v155
	v_mov_b32_e32 v171, v135
	v_cvt_pk_fp8_f32 v171, v214, v215
	v_med3_f32 v216, v216, s11, v155
	v_med3_f32 v217, v217, s11, v155
	v_cvt_pk_fp8_f32 v171, v216, v217 op_sel:[0,0,1]
	s_waitcnt lgkmcnt(6)
	v_pk_mul_f32 v[218:219], v[218:219], s[100:101]
	v_pk_mul_f32 v[220:221], v[220:221], s[100:101]
	v_med3_f32 v218, v218, s11, v155
	v_med3_f32 v219, v219, s11, v155
	v_mov_b32_e32 v172, v135
	v_cvt_pk_fp8_f32 v172, v218, v219
	v_med3_f32 v220, v220, s11, v155
	v_med3_f32 v221, v221, s11, v155
	v_cvt_pk_fp8_f32 v172, v220, v221 op_sel:[0,0,1]
	s_waitcnt lgkmcnt(4)
	v_pk_mul_f32 v[222:223], v[222:223], s[100:101]
	v_pk_mul_f32 v[224:225], v[224:225], s[100:101]
	v_med3_f32 v222, v222, s11, v155
	v_med3_f32 v223, v223, s11, v155
	v_mov_b32_e32 v173, v135
	v_cvt_pk_fp8_f32 v173, v222, v223
	v_med3_f32 v224, v224, s11, v155
	v_med3_f32 v225, v225, s11, v155
	v_cvt_pk_fp8_f32 v173, v224, v225 op_sel:[0,0,1]
	s_waitcnt lgkmcnt(2)
	v_pk_mul_f32 v[226:227], v[226:227], s[100:101]
	v_pk_mul_f32 v[228:229], v[228:229], s[100:101]
	v_med3_f32 v226, v226, s11, v155
	v_med3_f32 v227, v227, s11, v155
	v_mov_b32_e32 v174, v135
	v_cvt_pk_fp8_f32 v174, v226, v227
	v_med3_f32 v228, v228, s11, v155
	v_med3_f32 v229, v229, s11, v155
	v_cvt_pk_fp8_f32 v174, v228, v229 op_sel:[0,0,1]
	s_waitcnt lgkmcnt(0)
	v_pk_mul_f32 v[230:231], v[230:231], s[100:101]
	v_pk_mul_f32 v[232:233], v[232:233], s[100:101]
	v_med3_f32 v230, v230, s11, v155
	v_med3_f32 v231, v231, s11, v155
	v_mov_b32_e32 v175, v135
	v_cvt_pk_fp8_f32 v175, v230, v231
	v_med3_f32 v232, v232, s11, v155
	v_med3_f32 v233, v233, s11, v155
	v_cvt_pk_fp8_f32 v175, v232, v233 op_sel:[0,0,1]
	s_barrier
	ds_write_b128 v156, v[130:133]
	ds_write_b128 v157, v[164:167]
	ds_write_b128 v158, v[168:171]
	ds_write_b128 v159, v[172:175]
	s_waitcnt lgkmcnt(0)
	s_barrier
	ds_read_b128 v[130:133], v160
	v_add_u32_e32 v164, s4, v140
	s_cselect_b64 s[46:47], -1, 0
	s_mov_b64 s[2:3], -1
	s_and_b64 vcc, exec, s[46:47]
	v_lshlrev_b32_e32 v165, 1, v164
	v_add_u32_e32 v137, s0, v138
	s_cbranch_vccz .Lcv_380
	v_lshlrev_b32_e32 v134, 2, v164
	v_lshrrev_b32_e32 v166, 1, v164
	v_and_b32_e32 v167, 0xffffffe3, v164
	v_and_or_b32 v168, v166, 12, v167
	v_and_or_b32 v169, v134, 16, v167
	v_ashrrev_i32_e32 v166, 7, v164
	v_ashrrev_i32_e32 v134, 7, v137
	v_mad_u64_u32 v[166:167], s[2:3], v166, 56, v[134:135]
	v_lshrrev_b32_e32 v134, 3, v169
	v_bfe_u32 v169, v137, 6, 1
	v_ashrrev_i32_e32 v167, 31, v166
	v_and_or_b32 v134, v134, 14, v169
	v_lshlrev_b32_e32 v168, 6, v168
	v_and_b32_e32 v169, 63, v137
	v_lshlrev_b64 v[166:167], 14, v[166:167]
	v_and_or_b32 v168, v168, s68, v169
	v_lshlrev_b32_e32 v134, 10, v134
	v_and_b32_e32 v169, 32, v165
	v_bitop3_b32 v134, v134, v168, v169 bitop3:0xf6
	v_lshl_add_u64 v[166:167], s[6:7], 0, v[166:167]
	v_lshl_add_u64 v[166:167], v[166:167], 0, v[134:135]
	s_waitcnt lgkmcnt(0)
	global_store_dwordx4 v[166:167], v[130:133], off nt
	s_mov_b64 s[2:3], 0

.Lcv_moe_w2:
	ds_write_b128 v142, v[66:69]
	ds_write_b128 v142, v[70:73] offset:8192
	ds_write_b128 v142, v[74:77] offset:16384
	ds_write_b128 v142, v[78:81] offset:24576
	ds_write_b128 v142, v[82:85] offset:32768
	ds_write_b128 v142, v[86:89] offset:40960
	ds_write_b128 v142, v[90:93] offset:49152
	ds_write_b128 v142, v[94:97] offset:57344
	ds_write_b128 v143, v[98:101]
	ds_write_b128 v144, v[102:105]
	ds_write_b128 v145, v[106:109]
	ds_write_b128 v146, v[110:113]
	ds_write_b128 v147, v[114:117]
	ds_write_b128 v148, v[118:121]
	ds_write_b128 v149, v[122:125]
	ds_write_b128 v150, v[126:129]
	s_waitcnt lgkmcnt(0)
	s_barrier
	s_mov_b32 s100, 0x43000000
	s_mov_b32 s101, 0x43000000
	ds_read2st64_b32 v[202:203], v151 offset0:0 offset1:4
	ds_read2st64_b32 v[204:205], v151 offset0:8 offset1:12
	ds_read2st64_b32 v[206:207], v151 offset0:16 offset1:20
	ds_read2st64_b32 v[208:209], v151 offset0:24 offset1:28
	ds_read2st64_b32 v[210:211], v151 offset0:32 offset1:36
	ds_read2st64_b32 v[212:213], v151 offset0:40 offset1:44
	ds_read2st64_b32 v[214:215], v151 offset0:48 offset1:52
	ds_read2st64_b32 v[216:217], v151 offset0:56 offset1:60
	ds_read2st64_b32 v[218:219], v151 offset0:64 offset1:68
	ds_read2st64_b32 v[220:221], v151 offset0:72 offset1:76
	ds_read2st64_b32 v[222:223], v151 offset0:80 offset1:84
	ds_read2st64_b32 v[224:225], v151 offset0:88 offset1:92
	s_cmp_gt_i32 s69, 1
	s_waitcnt lgkmcnt(10)
	v_pk_mul_f32 v[202:203], v[202:203], s[100:101]
	v_pk_mul_f32 v[204:205], v[204:205], s[100:101]
	v_med3_f32 v202, v202, s11, v155
	v_med3_f32 v203, v203, s11, v155
	v_mov_b32_e32 v130, v135
	v_cvt_pk_fp8_f32 v130, v202, v203
	v_med3_f32 v204, v204, s11, v155
	v_med3_f32 v205, v205, s11, v155
	v_cvt_pk_fp8_f32 v130, v204, v205 op_sel:[0,0,1]
	ds_read2st64_b32 v[226:227], v151 offset0:96 offset1:100
	ds_read2st64_b32 v[228:229], v151 offset0:104 offset1:108
	s_waitcnt lgkmcnt(10)
	v_pk_mul_f32 v[206:207], v[206:207], s[100:101]
	v_pk_mul_f32 v[208:209], v[208:209], s[100:101]
	v_med3_f32 v206, v206, s11, v155
	v_med3_f32 v207, v207, s11, v155
	v_mov_b32_e32 v131, v135
	v_cvt_pk_fp8_f32 v131, v206, v207
	v_med3_f32 v208, v208, s11, v155
	v_med3_f32 v209, v209, s11, v155
	v_cvt_pk_fp8_f32 v131, v208, v209 op_sel:[0,0,1]
	ds_read2st64_b32 v[230:231], v151 offset0:112 offset1:116
	ds_read2st64_b32 v[232:233], v151 offset0:120 offset1:124
	s_waitcnt lgkmcnt(10)
	v_pk_mul_f32 v[210:211], v[210:211], s[100:101]
	v_pk_mul_f32 v[212:213], v[212:213], s[100:101]
	v_med3_f32 v210, v210, s11, v155
	v_med3_f32 v211, v211, s11, v155
	v_mov_b32_e32 v132, v135
	v_cvt_pk_fp8_f32 v132, v210, v211
	v_med3_f32 v212, v212, s11, v155
	v_med3_f32 v213, v213, s11, v155
	v_cvt_pk_fp8_f32 v132, v212, v213 op_sel:[0,0,1]
	ds_read2st64_b32 v[202:203], v151 offset0:128 offset1:132
	ds_read2st64_b32 v[204:205], v151 offset0:136 offset1:140
	s_waitcnt lgkmcnt(10)
	v_pk_mul_f32 v[214:215], v[214:215], s[100:101]
	v_pk_mul_f32 v[216:217], v[216:217], s[100:101]
	v_med3_f32 v214, v214, s11, v155
	v_med3_f32 v215, v215, s11, v155
	v_mov_b32_e32 v133, v135
	v_cvt_pk_fp8_f32 v133, v214, v215
	v_med3_f32 v216, v216, s11, v155
	v_med3_f32 v217, v217, s11, v155
	v_cvt_pk_fp8_f32 v133, v216, v217 op_sel:[0,0,1]
	ds_read2st64_b32 v[206:207], v151 offset0:144 offset1:148
	ds_read2st64_b32 v[208:209], v151 offset0:152 offset1:156
	s_waitcnt lgkmcnt(10)
	v_pk_mul_f32 v[218:219], v[218:219], s[100:101]
	v_pk_mul_f32 v[220:221], v[220:221], s[100:101]
	v_med3_f32 v218, v218, s11, v155
	v_med3_f32 v219, v219, s11, v155
	v_mov_b32_e32 v164, v135
	v_cvt_pk_fp8_f32 v164, v218, v219
	v_med3_f32 v220, v220, s11, v155
	v_med3_f32 v221, v221, s11, v155
	v_cvt_pk_fp8_f32 v164, v220, v221 op_sel:[0,0,1]
	ds_read2st64_b32 v[210:211], v151 offset0:160 offset1:164
	ds_read2st64_b32 v[212:213], v151 offset0:168 offset1:172
	s_waitcnt lgkmcnt(10)
	v_pk_mul_f32 v[222:223], v[222:223], s[100:101]
	v_pk_mul_f32 v[224:225], v[224:225], s[100:101]
	v_med3_f32 v222, v222, s11, v155
	v_med3_f32 v223, v223, s11, v155
	v_mov_b32_e32 v165, v135
	v_cvt_pk_fp8_f32 v165, v222, v223
	v_med3_f32 v224, v224, s11, v155
	v_med3_f32 v225, v225, s11, v155
	v_cvt_pk_fp8_f32 v165, v224, v225 op_sel:[0,0,1]
	ds_read2st64_b32 v[214:215], v151 offset0:176 offset1:180
	ds_read2st64_b32 v[216:217], v151 offset0:184 offset1:188
	s_waitcnt lgkmcnt(10)
	v_pk_mul_f32 v[226:227], v[226:227], s[100:101]
	v_pk_mul_f32 v[228:229], v[228:229], s[100:101]
	v_med3_f32 v226, v226, s11, v155
	v_med3_f32 v227, v227, s11, v155
	v_mov_b32_e32 v166, v135
	v_cvt_pk_fp8_f32 v166, v226, v227
	v_med3_f32 v228, v228, s11, v155
	v_med3_f32 v229, v229, s11, v155
	v_cvt_pk_fp8_f32 v166, v228, v229 op_sel:[0,0,1]
	ds_read2st64_b32 v[218:219], v151 offset0:192 offset1:196
	ds_read2st64_b32 v[220:221], v151 offset0:200 offset1:204
	s_waitcnt lgkmcnt(10)
	v_pk_mul_f32 v[230:231], v[230:231], s[100:101]
	v_pk_mul_f32 v[232:233], v[232:233], s[100:101]
	v_med3_f32 v230, v230, s11, v155
	v_med3_f32 v231, v231, s11, v155
	v_mov_b32_e32 v167, v135
	v_cvt_pk_fp8_f32 v167, v230, v231
	v_med3_f32 v232, v232, s11, v155
	v_med3_f32 v233, v233, s11, v155
	v_cvt_pk_fp8_f32 v167, v232, v233 op_sel:[0,0,1]
	ds_read2st64_b32 v[222:223], v151 offset0:208 offset1:212
	ds_read2st64_b32 v[224:225], v151 offset0:216 offset1:220
	s_waitcnt lgkmcnt(10)
	v_pk_mul_f32 v[202:203], v[202:203], s[100:101]
	v_pk_mul_f32 v[204:205], v[204:205], s[100:101]
	v_med3_f32 v202, v202, s11, v155
	v_med3_f32 v203, v203, s11, v155
	v_mov_b32_e32 v168, v135
	v_cvt_pk_fp8_f32 v168, v202, v203
	v_med3_f32 v204, v204, s11, v155
	v_med3_f32 v205, v205, s11, v155
	v_cvt_pk_fp8_f32 v168, v204, v205 op_sel:[0,0,1]
	ds_read2st64_b32 v[226:227], v151 offset0:224 offset1:228
	ds_read2st64_b32 v[228:229], v151 offset0:232 offset1:236
	s_waitcnt lgkmcnt(10)
	v_pk_mul_f32 v[206:207], v[206:207], s[100:101]
	v_pk_mul_f32 v[208:209], v[208:209], s[100:101]
	v_med3_f32 v206, v206, s11, v155
	v_med3_f32 v207, v207, s11, v155
	v_mov_b32_e32 v169, v135
	v_cvt_pk_fp8_f32 v169, v206, v207
	v_med3_f32 v208, v208, s11, v155
	v_med3_f32 v209, v209, s11, v155
	v_cvt_pk_fp8_f32 v169, v208, v209 op_sel:[0,0,1]
	ds_read2st64_b32 v[230:231], v151 offset0:240 offset1:244
	ds_read2st64_b32 v[232:233], v151 offset0:248 offset1:252
	s_waitcnt lgkmcnt(10)
	v_pk_mul_f32 v[210:211], v[210:211], s[100:101]
	v_pk_mul_f32 v[212:213], v[212:213], s[100:101]
	v_med3_f32 v210, v210, s11, v155
	v_med3_f32 v211, v211, s11, v155
	v_mov_b32_e32 v170, v135
	v_cvt_pk_fp8_f32 v170, v210, v211
	v_med3_f32 v212, v212, s11, v155
	v_med3_f32 v213, v213, s11, v155
	v_cvt_pk_fp8_f32 v170, v212, v213 op_sel:[0,0,1]
	s_waitcnt lgkmcnt(8)
	v_pk_mul_f32 v[214:215], v[214:215], s[100:101]
	v_pk_mul_f32 v[216:217], v[216:217], s[100:101]
	v_med3_f32 v214, v214, s11, v155
	v_med3_f32 v215, v215, s11, v155
	v_mov_b32_e32 v171, v135
	v_cvt_pk_fp8_f32 v171, v214, v215
	v_med3_f32 v216, v216, s11, v155
	v_med3_f32 v217, v217, s11, v155
	v_cvt_pk_fp8_f32 v171, v216, v217 op_sel:[0,0,1]
	s_waitcnt lgkmcnt(6)
	v_pk_mul_f32 v[218:219], v[218:219], s[100:101]
	v_pk_mul_f32 v[220:221], v[220:221], s[100:101]
	v_med3_f32 v218, v218, s11, v155
	v_med3_f32 v219, v219, s11, v155
	v_mov_b32_e32 v172, v135
	v_cvt_pk_fp8_f32 v172, v218, v219
	v_med3_f32 v220, v220, s11, v155
	v_med3_f32 v221, v221, s11, v155
	v_cvt_pk_fp8_f32 v172, v220, v221 op_sel:[0,0,1]
	s_waitcnt lgkmcnt(4)
	v_pk_mul_f32 v[222:223], v[222:223], s[100:101]
	v_pk_mul_f32 v[224:225], v[224:225], s[100:101]
	v_med3_f32 v222, v222, s11, v155
	v_med3_f32 v223, v223, s11, v155
	v_mov_b32_e32 v173, v135
	v_cvt_pk_fp8_f32 v173, v222, v223
	v_med3_f32 v224, v224, s11, v155
	v_med3_f32 v225, v225, s11, v155
	v_cvt_pk_fp8_f32 v173, v224, v225 op_sel:[0,0,1]
	s_waitcnt lgkmcnt(2)
	v_pk_mul_f32 v[226:227], v[226:227], s[100:101]
	v_pk_mul_f32 v[228:229], v[228:229], s[100:101]
	v_med3_f32 v226, v226, s11, v155
	v_med3_f32 v227, v227, s11, v155
	v_mov_b32_e32 v174, v135
	v_cvt_pk_fp8_f32 v174, v226, v227
	v_med3_f32 v228, v228, s11, v155
	v_med3_f32 v229, v229, s11, v155
	v_cvt_pk_fp8_f32 v174, v228, v229 op_sel:[0,0,1]
	s_waitcnt lgkmcnt(0)
	v_pk_mul_f32 v[230:231], v[230:231], s[100:101]
	v_pk_mul_f32 v[232:233], v[232:233], s[100:101]
	v_med3_f32 v230, v230, s11, v155
	v_med3_f32 v231, v231, s11, v155
	v_mov_b32_e32 v175, v135
	v_cvt_pk_fp8_f32 v175, v230, v231
	v_med3_f32 v232, v232, s11, v155
	v_med3_f32 v233, v233, s11, v155
	v_cvt_pk_fp8_f32 v175, v232, v233 op_sel:[0,0,1]
	s_barrier
	ds_write_b128 v156, v[130:133]
	ds_write_b128 v157, v[164:167]
	ds_write_b128 v158, v[168:171]
	ds_write_b128 v159, v[172:175]
	s_waitcnt lgkmcnt(0)
	s_barrier
	ds_read_b128 v[130:133], v160
	v_add_u32_e32 v164, s72, v140
	s_cselect_b64 s[44:45], -1, 0
	s_mov_b64 s[2:3], -1
	s_and_b64 vcc, exec, s[44:45]
	v_lshlrev_b32_e32 v165, 1, v164
	v_add_u32_e32 v137, s14, v138
	s_cbranch_vccz .Lcv_404
	v_lshlrev_b32_e32 v134, 2, v164
	v_lshrrev_b32_e32 v166, 1, v164
	v_and_b32_e32 v167, 0xffffffe3, v164
	v_and_or_b32 v168, v166, 12, v167
	v_and_or_b32 v169, v134, 16, v167
	v_ashrrev_i32_e32 v166, 7, v164
	v_ashrrev_i32_e32 v134, 7, v137
	v_mad_u64_u32 v[166:167], s[2:3], v166, 56, v[134:135]
	v_lshrrev_b32_e32 v134, 3, v169
	v_bfe_u32 v169, v137, 6, 1
	v_ashrrev_i32_e32 v167, 31, v166
	v_and_or_b32 v134, v134, 14, v169
	v_lshlrev_b32_e32 v168, 6, v168
	v_and_b32_e32 v169, 63, v137
	v_lshlrev_b64 v[166:167], 14, v[166:167]
	v_and_or_b32 v168, v168, s68, v169
	v_lshlrev_b32_e32 v134, 10, v134
	v_and_b32_e32 v169, 32, v165
	v_bitop3_b32 v134, v134, v168, v169 bitop3:0xf6
	v_lshl_add_u64 v[166:167], s[40:41], 0, v[166:167]
	v_lshl_add_u64 v[166:167], v[166:167], 0, v[134:135]
	s_waitcnt lgkmcnt(0)
	global_store_dwordx4 v[166:167], v[130:133], off nt
	s_mov_b64 s[2:3], 0
